# baseline (speedup 1.0000x reference)
_Z6gat_k2PKDF16_S0_S0_PKfPf:
	s_load_dwordx8 s[4:11], s[0:1], 0x0
	s_load_dwordx2 s[12:13], s[0:1], 0x20
	v_readfirstlane_b32 s14, v0
	v_and_b32_e32 v46, 63, v0
	v_lshlrev_b32_e32 v1, 4, v46
	s_and_b32 s16, s2, 1
	s_bfe_u32 s17, s2, 0x60003
	s_lshr_b32 s18, s2, 1
	s_lshr_b32 s15, s14, 6
	s_lshl_b32 s19, s16, 19
	s_lshl_b32 s23, s15, 16
	s_add_u32 s19, s19, s23
	s_lshl_b32 s23, s15, 11
	v_lshrrev_b32_e32 v48, 1, v46
	v_add_u32_e32 v48, s17, v48
	v_and_b32_e32 v48, 63, v48
	v_lshlrev_b32_e32 v48, 5, v48
	v_and_b32_e32 v49, 1, v46
	v_lshl_or_b32 v48, v49, 4, v48
	v_xor_b32_e32 v49, 0x400, v48
	v_add_u32_e32 v48, s23, v48
	v_add_u32_e32 v49, s23, v49
	s_mul_i32 s32, s15, 0x1900
	s_add_u32 s32, s32, 75776
	v_and_b32_e32 v44, 31, v0
	v_lshlrev_b32_e32 v45, 2, v44
	s_lshl_b32 s23, s18, 8
	v_add_u32_e32 v45, s23, v45
	s_waitcnt lgkmcnt(0)
	global_load_dword v42, v45, s[10:11]
	global_load_dword v43, v45, s[10:11] offset:128
	s_mov_b32 m0, s32
	s_add_u32 s33, s32, 0x400
	global_load_lds_dwordx4 v48, s[6:7]
	s_mov_b32 m0, s33
	s_add_u32 s34, s32, 0x800
	global_load_lds_dwordx4 v49, s[6:7]
	s_mov_b32 m0, s34
	s_add_u32 s35, s32, 0xc00
	global_load_lds_dwordx4 v48, s[8:9]
	s_mov_b32 m0, s35
	s_nop 0
	global_load_lds_dwordx4 v49, s[8:9]
	s_add_u32 s20, s4, s19
	s_addc_u32 s21, s5, 0
	s_add_u32 s23, s17, 0
	s_and_b32 s23, s23, 63
	s_lshl_b32 s23, s23, 10
	s_add_u32 s24, s20, s23
	s_addc_u32 s25, s21, 0
	global_load_dwordx4 v[64:67], v1, s[24:25]
	s_add_u32 s23, s17, 1
	s_and_b32 s23, s23, 63
	s_lshl_b32 s23, s23, 10
	s_add_u32 s24, s20, s23
	s_addc_u32 s25, s21, 0
	global_load_dwordx4 v[68:71], v1, s[24:25]
	s_add_u32 s23, s17, 2
	s_and_b32 s23, s23, 63
	s_lshl_b32 s23, s23, 10
	s_add_u32 s24, s20, s23
	s_addc_u32 s25, s21, 0
	global_load_dwordx4 v[72:75], v1, s[24:25]
	s_add_u32 s23, s17, 3
	s_and_b32 s23, s23, 63
	s_lshl_b32 s23, s23, 10
	s_add_u32 s24, s20, s23
	s_addc_u32 s25, s21, 0
	global_load_dwordx4 v[76:79], v1, s[24:25]
	s_add_u32 s23, s17, 4
	s_and_b32 s23, s23, 63
	s_lshl_b32 s23, s23, 10
	s_add_u32 s24, s20, s23
	s_addc_u32 s25, s21, 0
	global_load_dwordx4 v[80:83], v1, s[24:25]
	s_add_u32 s23, s17, 5
	s_and_b32 s23, s23, 63
	s_lshl_b32 s23, s23, 10
	s_add_u32 s24, s20, s23
	s_addc_u32 s25, s21, 0
	global_load_dwordx4 v[84:87], v1, s[24:25]
	s_add_u32 s23, s17, 6
	s_and_b32 s23, s23, 63
	s_lshl_b32 s23, s23, 10
	s_add_u32 s24, s20, s23
	s_addc_u32 s25, s21, 0
	global_load_dwordx4 v[88:91], v1, s[24:25]
	s_add_u32 s23, s17, 7
	s_and_b32 s23, s23, 63
	s_lshl_b32 s23, s23, 10
	s_add_u32 s24, s20, s23
	s_addc_u32 s25, s21, 0
	global_load_dwordx4 v[92:95], v1, s[24:25]
	v_accvgpr_write_b32 a0, 0
	v_accvgpr_write_b32 a1, 0
	v_accvgpr_write_b32 a2, 0
	v_accvgpr_write_b32 a3, 0
	v_accvgpr_write_b32 a4, 0
	v_accvgpr_write_b32 a5, 0
	v_accvgpr_write_b32 a6, 0
	v_accvgpr_write_b32 a7, 0
	v_accvgpr_write_b32 a8, 0
	v_accvgpr_write_b32 a9, 0
	v_accvgpr_write_b32 a10, 0
	v_accvgpr_write_b32 a11, 0
	v_accvgpr_write_b32 a12, 0
	v_accvgpr_write_b32 a13, 0
	v_accvgpr_write_b32 a14, 0
	v_accvgpr_write_b32 a15, 0
	v_accvgpr_write_b32 a16, 0
	v_accvgpr_write_b32 a17, 0
	v_accvgpr_write_b32 a18, 0
	v_accvgpr_write_b32 a19, 0
	v_accvgpr_write_b32 a20, 0
	v_accvgpr_write_b32 a21, 0
	v_accvgpr_write_b32 a22, 0
	v_accvgpr_write_b32 a23, 0
	v_accvgpr_write_b32 a24, 0
	v_accvgpr_write_b32 a25, 0
	v_accvgpr_write_b32 a26, 0
	v_accvgpr_write_b32 a27, 0
	v_accvgpr_write_b32 a28, 0
	v_accvgpr_write_b32 a29, 0
	v_accvgpr_write_b32 a30, 0
	v_accvgpr_write_b32 a31, 0
	v_accvgpr_write_b32 a32, 0
	v_accvgpr_write_b32 a33, 0
	v_accvgpr_write_b32 a34, 0
	v_accvgpr_write_b32 a35, 0
	v_accvgpr_write_b32 a36, 0
	v_accvgpr_write_b32 a37, 0
	v_accvgpr_write_b32 a38, 0
	v_accvgpr_write_b32 a39, 0
	v_mov_b32_e32 v2, 0
	v_mov_b32_e32 v3, 0
	v_mov_b32_e32 v4, 0
	v_mov_b32_e32 v5, 0
	v_add_u32_e32 v47, s32, v1
	ds_write_b128 v47, v[2:5] offset:4096
	ds_write_b128 v47, v[2:5] offset:5120
	s_waitcnt vmcnt(8)
	v_cvt_f16_f32_e32 v42, v42
	v_cvt_f16_f32_e32 v43, v43
	s_mov_b32 s28, 0x5040100
	v_perm_b32 v42, v42, v42, s28
	v_perm_b32 v43, v43, v43, s28
	v_lshrrev_b32_e32 v44, 5, v46
	v_and_b32_e32 v45, 15, v46
	v_bfe_u32 v47, v46, 4, 1
	v_cmp_eq_u32_e32 vcc, v45, v47
	v_lshlrev_b32_e32 v44, 4, v44
	v_add_u32_e32 v46, s32, v44
	v_add_u32_e32 v45, 0x800, v46
	v_mov_b32_e32 v47, s32
	v_add_u32_e32 v47, 0x1000, v47
	v_cndmask_b32_e32 v47, v47, v45, vcc
	s_waitcnt lgkmcnt(0)
	ds_read_b128 v[144:147], v46
	ds_read_b128 v[148:151], v46 offset:32
	ds_read_b128 v[160:163], v47
	ds_read_b128 v[152:155], v46 offset:64
	ds_read_b128 v[164:167], v47 offset:32
	s_add_u32 s27, s17, 8
	s_lshl_b32 s27, s27, 10
	s_add_u32 s29, s17, 63
	s_lshl_b32 s29, s29, 10
	s_movk_i32 s28, 0x400
	s_mov_b32 s26, 0
	s_waitcnt lgkmcnt(4)
	v_pk_max_u16 v128, v144, v42
	v_pk_max_u16 v129, v145, v42
	v_pk_max_u16 v130, v146, v42
	v_pk_max_u16 v131, v147, v42
	v_pk_max_u16 v136, v144, v43
	v_pk_max_u16 v137, v145, v43
	v_pk_max_u16 v138, v146, v43
	v_pk_max_u16 v139, v147, v43
	s_mov_b32 s31, 0xfc00
	s_cmp_ge_u32 s15, 4
	s_cbranch_scc0 .Lk2_noprio
	s_setprio 1
